# v14: + P4 side job staged in VGPRs and its finish/issue moved into the MFMA blocks (m1)
# baseline (speedup 1.0000x reference)
.LBB0_523:
	s_andn2_b64 vcc, exec, s[4:5]
	s_cbranch_vccnz .LBB0_554
	s_andn2_b64 vcc, exec, s[2:3]
	v_readfirstlane_b32 s3, v0
	s_cbranch_vccnz .LBB0_554
	s_lshr_b32 s7, s3, 6
	s_lshr_b32 s6, s3, 8
	s_lshl_b32 s8, s7, 10
	s_and_b64 s[0:1], s[0:1], exec
	s_cselect_b32 s0, s42, s41
	s_add_i32 s0, s0, s33
	s_ashr_i32 s1, s0, 31
	s_lshr_b32 s1, s1, 26
	s_add_i32 s1, s0, s1
	s_ashr_i32 s2, s1, 6
	s_and_b32 s1, s1, 0xffc0
	s_sub_i32 s0, s0, s1
	s_bfe_i32 s1, s0, 0x80000
	s_bfe_u32 s1, s1, 0x3000c
	s_add_i32 s1, s0, s1
	s_lshl_b32 s4, s2, 3
	s_bfe_i32 s2, s1, 0x80000
	s_and_b32 s1, s1, 0xf8
	s_sub_i32 s0, s0, s1
	s_sext_i32_i16 s2, s2
	s_sext_i32_i8 s0, s0
	s_lshr_b32 s2, s2, 3
	s_add_i32 s20, s4, s0
	s_ashr_i32 s21, s20, 31
	s_bfe_i64 s[4:5], s[2:3], 0x100000
	s_lshl_b64 s[0:1], s[20:21], 20
	s_lshl_b64 s[4:5], s[4:5], 20
	s_add_u32 s4, s30, s4
	s_addc_u32 s5, s31, s5
	s_add_i32 s21, s8, 0
	s_add_i32 s33, s21, 0x10000
	s_add_i32 s36, s21, 0x12000
	v_lshl_add_u64 v[2:3], s[4:5], 0, v[210:211]
	s_mov_b32 m0, s33
	s_add_u32 s8, s4, 0x80000
	global_load_lds_dwordx4 v[2:3], off
	v_lshl_add_u64 v[4:5], s[4:5], 0, v[212:213]
	s_mov_b32 m0, s36
	s_addc_u32 s9, s5, 0
	s_add_i32 s37, s21, 0x14000
	s_add_i32 s41, s21, 0x16000
	global_load_lds_dwordx4 v[4:5], off
	v_lshl_add_u64 v[6:7], s[8:9], 0, v[210:211]
	s_mov_b32 m0, s37
	s_add_u32 s24, s38, s0
	global_load_lds_dwordx4 v[6:7], off
	v_lshl_add_u64 v[6:7], s[8:9], 0, v[212:213]
	s_mov_b32 m0, s41
	s_addc_u32 s25, s39, s1
	s_add_i32 s43, s21, 0x2000
	global_load_lds_dwordx4 v[6:7], off
	v_lshl_add_u64 v[8:9], s[24:25], 0, v[210:211]
	s_mov_b32 m0, s21
	s_add_u32 s0, s24, 0x80000
	global_load_lds_dwordx4 v[8:9], off
	v_lshl_add_u64 v[6:7], s[24:25], 0, v[212:213]
	s_mov_b32 m0, s43
	s_addc_u32 s1, s25, 0
	s_add_i32 s44, s21, 0x4000
	global_load_lds_dwordx4 v[6:7], off
	v_lshl_add_u64 v[10:11], s[0:1], 0, v[210:211]
	s_mov_b32 m0, s44
	s_add_i32 s46, s21, 0x6000
	global_load_lds_dwordx4 v[10:11], off
	v_lshl_add_u64 v[10:11], s[0:1], 0, v[212:213]
	s_mov_b32 m0, s46
	s_cmp_lg_u32 s6, 1
	global_load_lds_dwordx4 v[10:11], off
	s_mov_b32 s42, 0
	s_mov_b32 s98, -1
	s_mov_b32 s99, -1
	s_mov_b32 s100, 0
	s_cbranch_scc1 .LBB0_527
	s_barrier

.Lp4vg_mmafter_b:
	s_barrier
	s_mov_b32 m0, s48
	v_lshl_add_u64 v[4:5], v[4:5], 0, s[0:1]
	s_add_u32 s4, s34, 0x80080
	ds_read_b128 v[174:177], v230 offset:49152
	ds_read_b128 v[178:181], v230 offset:50176
	ds_read_b128 v[182:185], v230 offset:51200
	ds_read_b128 v[186:189], v230 offset:52224
	ds_read_b128 v[190:193], v230 offset:53248
	ds_read_b128 v[194:197], v230 offset:54272
	ds_read_b128 v[198:201], v230 offset:55296
	ds_read_b128 v[202:205], v230 offset:56320
	global_load_lds_dwordx4 v[4:5], off
	v_lshl_add_u64 v[4:5], v[222:223], 0, s[0:1]
	s_mov_b32 m0, s49
	s_addc_u32 s5, s35, 0
	global_load_lds_dwordx4 v[4:5], off
	v_lshl_add_u64 v[4:5], s[4:5], 0, v[210:211]
	s_mov_b32 m0, s52
	s_nop 0
	global_load_lds_dwordx4 v[4:5], off
	v_lshl_add_u64 v[4:5], s[4:5], 0, v[212:213]
	s_mov_b32 m0, s53
	s_nop 0
	global_load_lds_dwordx4 v[4:5], off
	v_lshl_add_u64 v[4:5], v[224:225], 0, s[0:1]
	s_mov_b32 m0, s50
	s_nop 0
	global_load_lds_dwordx4 v[4:5], off
	v_lshl_add_u64 v[4:5], v[226:227], 0, s[0:1]
	s_mov_b32 m0, s51
	s_nop 0
	global_load_lds_dwordx4 v[4:5], off
	s_cmp_eq_u32 s100, 3
	s_cbranch_scc1 .Lp4vg_w11_b2
	s_waitcnt vmcnt(8)
	s_branch .Lp4vg_wd_b2

.Lp4vg_wd_b2:
	s_waitcnt lgkmcnt(0)
	s_barrier
	s_setprio 1
	s_waitcnt lgkmcnt(0)
	v_mfma_f32_16x16x32_bf16 v[74:77], v[158:161], v[174:177], v[74:77]
	v_mfma_f32_16x16x32_bf16 v[70:73], v[166:169], v[174:177], v[70:73]
	v_mfma_f32_16x16x32_bf16 v[62:65], v[158:161], v[182:185], v[62:65]
	v_mfma_f32_16x16x32_bf16 v[58:61], v[166:169], v[182:185], v[58:61]
	v_mfma_f32_16x16x32_bf16 v[46:49], v[158:161], v[190:193], v[46:49]
	v_mfma_f32_16x16x32_bf16 v[42:45], v[166:169], v[190:193], v[42:45]
	v_mfma_f32_16x16x32_bf16 v[30:33], v[158:161], v[198:201], v[30:33]
	v_mfma_f32_16x16x32_bf16 v[26:29], v[166:169], v[198:201], v[26:29]
	v_mfma_f32_16x16x32_bf16 v[74:77], v[162:165], v[178:181], v[74:77]
	v_mfma_f32_16x16x32_bf16 v[70:73], v[170:173], v[178:181], v[70:73]
	v_mfma_f32_16x16x32_bf16 v[62:65], v[162:165], v[186:189], v[62:65]
	v_mfma_f32_16x16x32_bf16 v[58:61], v[170:173], v[186:189], v[58:61]
	v_mfma_f32_16x16x32_bf16 v[46:49], v[162:165], v[194:197], v[46:49]
	v_mfma_f32_16x16x32_bf16 v[42:45], v[170:173], v[194:197], v[42:45]
	v_mfma_f32_16x16x32_bf16 v[30:33], v[162:165], v[202:205], v[30:33]
	v_mfma_f32_16x16x32_bf16 v[26:29], v[170:173], v[202:205], v[26:29]
	s_setprio 0
	s_setprio 1
	v_mfma_f32_16x16x32_bf16 v[66:69], v[142:145], v[174:177], v[66:69]
	v_mfma_f32_16x16x32_bf16 v[54:57], v[150:153], v[174:177], v[54:57]
	v_mfma_f32_16x16x32_bf16 v[50:53], v[142:145], v[182:185], v[50:53]
	v_mfma_f32_16x16x32_bf16 v[38:41], v[150:153], v[182:185], v[38:41]
	v_mfma_f32_16x16x32_bf16 v[34:37], v[142:145], v[190:193], v[34:37]
	v_mfma_f32_16x16x32_bf16 v[22:25], v[150:153], v[190:193], v[22:25]
	v_mfma_f32_16x16x32_bf16 v[18:21], v[142:145], v[198:201], v[18:21]
	v_mfma_f32_16x16x32_bf16 v[14:17], v[150:153], v[198:201], v[14:17]
	v_mfma_f32_16x16x32_bf16 v[66:69], v[146:149], v[178:181], v[66:69]
	v_mfma_f32_16x16x32_bf16 v[54:57], v[154:157], v[178:181], v[54:57]
	v_mfma_f32_16x16x32_bf16 v[50:53], v[146:149], v[186:189], v[50:53]
	v_mfma_f32_16x16x32_bf16 v[38:41], v[154:157], v[186:189], v[38:41]
	v_mfma_f32_16x16x32_bf16 v[34:37], v[146:149], v[194:197], v[34:37]
	v_mfma_f32_16x16x32_bf16 v[22:25], v[154:157], v[194:197], v[22:25]
	v_mfma_f32_16x16x32_bf16 v[18:21], v[146:149], v[202:205], v[18:21]
	v_mfma_f32_16x16x32_bf16 v[14:17], v[154:157], v[202:205], v[14:17]
	s_setprio 0
	s_barrier
	s_add_i32 s60, s60, 2
	s_add_u32 s24, s24, 0x100
	s_addc_u32 s25, s25, 0
	s_add_u32 s58, s58, 0x100
	s_addc_u32 s59, s59, 0
	s_cmp_gt_u32 s60, 29
	s_cbranch_scc1 .LBB0_548
.LBB0_536:
	ds_read_b128 v[158:161], v228
	ds_read_b128 v[162:165], v228 offset:1024
	ds_read_b128 v[166:169], v228 offset:2048
	ds_read_b128 v[170:173], v228 offset:3072
	ds_read_b128 v[142:145], v229
	ds_read_b128 v[146:149], v229 offset:1024
	ds_read_b128 v[150:153], v229 offset:2048
	ds_read_b128 v[154:157], v229 offset:3072
	v_lshl_add_u64 v[4:5], s[24:25], 0, v[214:215]
	s_add_i32 m0, s21, 0xc000
	ds_read_b128 v[198:201], v230
	ds_read_b128 v[202:205], v230 offset:1024
	ds_read_b128 v[190:193], v230 offset:2048
	ds_read_b128 v[194:197], v230 offset:3072
	ds_read_b128 v[182:185], v230 offset:4096
	ds_read_b128 v[186:189], v230 offset:5120
	ds_read_b128 v[174:177], v230 offset:6144
	ds_read_b128 v[178:181], v230 offset:7168
	global_load_lds_dwordx4 v[4:5], off
	v_lshl_add_u64 v[4:5], s[24:25], 0, v[216:217]
	s_add_i32 m0, s21, 0xe000
	s_nop 0
	global_load_lds_dwordx4 v[4:5], off
	s_cmp_eq_u32 s100, 3
	s_cbranch_scc1 .Lp4vg_w11_a1
	s_waitcnt vmcnt(8)
	s_branch .Lp4vg_wd_a1

;     __device__ __forceinline__ void finish(v4i_t& t0, v4i_t& t1, int j, int tid) const {
;         asm volatile("" : "+v"(t0), "+v"(t1));
;         const float* s0; unsigned char* d; addr(j, tid, s0, d);
;         const f32x4 r0 = __builtin_bit_cast(f32x4, t0) * 64.f, r1 = __builtin_bit_cast(f32x4, t1) * 64.f;
;         int w0 = 0, w1 = 0; w0 = __builtin_amdgcn_cvt_pk_fp8_f32(r0[0], r1[0], w0, false); w0 = __builtin_amdgcn_cvt_pk_fp8_f32(r0[1], r1[1], w0, true);
;         w1 = __builtin_amdgcn_cvt_pk_fp8_f32(r0[2], r1[2], w1, false); w1 = __builtin_amdgcn_cvt_pk_fp8_f32(r0[3], r1[3], w1, true);
;         typedef int v2is __attribute__((ext_vector_type(2))); __builtin_nontemporal_store((v2is){w0, w1}, (v2is*)d);
.Lp4vg_wd_a1:
	s_waitcnt lgkmcnt(0)
	s_barrier
	s_cmp_lt_i32 s98, 0
	s_cbranch_scc1 .Lp4vg_mmslow_a
	s_cmp_gt_i32 s42, 31
	s_cbranch_scc1 .Lp4vg_mmslow_a
	s_setprio 1
	s_waitcnt lgkmcnt(0)
	v_mfma_f32_16x16x32_bf16 v[138:141], v[158:161], v[198:201], v[138:141]
	s_add_i32 s22, s98, s47
	s_lshr_b32 s4, s22, 31
	s_add_i32 s4, s22, s4
	v_mfma_f32_16x16x32_bf16 v[134:137], v[166:169], v[198:201], v[134:137]
	s_ashr_i32 s23, s4, 1
	s_ashr_i32 s4, s4, 11
	s_and_b32 s5, s23, 0x3ff
	v_mfma_f32_16x16x32_bf16 v[126:129], v[158:161], v[190:193], v[126:129]
	s_ashr_i32 s34, s4, 31
	s_lshl_b32 s4, s4, 10
	v_pk_mul_f32 v[6:7], v[6:7], s[2:3] op_sel_hi:[1,0]
	v_mfma_f32_16x16x32_bf16 v[122:125], v[166:169], v[190:193], v[122:125]
	v_pk_mul_f32 v[8:9], v[8:9], s[2:3] op_sel_hi:[1,0]
	v_pk_mul_f32 v[10:11], v[10:11], s[2:3] op_sel_hi:[1,0]
	v_pk_mul_f32 v[12:13], v[12:13], s[2:3] op_sel_hi:[1,0]
	v_mfma_f32_16x16x32_bf16 v[110:113], v[158:161], v[182:185], v[110:113]
	s_or_b32 s4, s4, s5
	v_cvt_pk_fp8_f32 v6, v6, v10
	s_mul_hi_u32 s5, s4, 0x2100
	v_mfma_f32_16x16x32_bf16 v[106:109], v[166:169], v[182:185], v[106:109]
	s_mulk_i32 s34, 0x2100
	v_cvt_pk_fp8_f32 v6, v7, v11 op_sel:[0,0,1]
	s_add_i32 s5, s5, s34
	v_mfma_f32_16x16x32_bf16 v[94:97], v[158:161], v[174:177], v[94:97]
	s_mulk_i32 s4, 0x2100
	v_cvt_pk_fp8_f32 v7, v8, v12
	v_readlane_b32 s101, v251, 49
	v_mfma_f32_16x16x32_bf16 v[90:93], v[166:169], v[174:177], v[90:93]
	s_add_u32 s4, s101, s4
	v_readlane_b32 s101, v251, 31
	s_addc_u32 s5, s101, s5
	v_mfma_f32_16x16x32_bf16 v[138:141], v[162:165], v[202:205], v[138:141]
	v_cvt_pk_fp8_f32 v7, v9, v13 op_sel:[0,0,1]
	v_lshl_or_b32 v222, s22, 11, v208
	s_lshl_b32 s34, s23, 12
	v_mfma_f32_16x16x32_bf16 v[134:137], v[170:173], v[202:205], v[134:137]
	v_subrev_u32_e32 v4, s34, v222
	v_ashrrev_i32_e32 v5, 31, v4
	v_lshl_add_u64 v[4:5], v[4:5], 1, s[4:5]
	v_mfma_f32_16x16x32_bf16 v[126:129], v[162:165], v[194:197], v[126:129]
	global_store_dwordx2 v[4:5], v[6:7], off nt
	s_add_i32 s22, s42, s47
	s_lshr_b32 s4, s22, 31
	v_mfma_f32_16x16x32_bf16 v[122:125], v[170:173], v[194:197], v[122:125]
	s_add_i32 s4, s22, s4
	s_ashr_i32 s23, s4, 1
	s_ashr_i32 s4, s4, 11
	v_mfma_f32_16x16x32_bf16 v[110:113], v[162:165], v[186:189], v[110:113]
	s_ashr_i32 s5, s4, 31
	s_lshl_b64 s[4:5], s[4:5], 25
	v_readlane_b32 s34, v251, 36
	v_mfma_f32_16x16x32_bf16 v[106:109], v[170:173], v[186:189], v[106:109]
	v_readlane_b32 s35, v251, 37
	s_add_u32 s4, s34, s4
	s_addc_u32 s5, s35, s5
	v_mfma_f32_16x16x32_bf16 v[94:97], v[162:165], v[178:181], v[94:97]
	s_lshl_b32 s34, s23, 15
	s_and_b32 s34, s34, 0x1ff8000
	s_add_u32 s34, s4, s34
	s_addc_u32 s35, s5, 0
	v_mfma_f32_16x16x32_bf16 v[90:93], v[170:173], v[178:181], v[90:93]
	s_setprio 0
	s_setprio 1
	s_lshl_b32 s4, s23, 12
	s_lshl_b32 s5, s22, 11
	s_sub_i32 s4, s5, s4
	v_mfma_f32_16x16x32_bf16 v[130:133], v[142:145], v[198:201], v[130:133]
	s_ashr_i32 s5, s4, 31
	s_lshl_b64 s[4:5], s[4:5], 2
	s_add_u32 s4, s34, s4
	s_addc_u32 s5, s35, s5
	v_mfma_f32_16x16x32_bf16 v[118:121], v[150:153], v[198:201], v[118:121]
	v_lshlrev_b32_e32 v2, 2, v208
	v_lshl_add_u64 v[4:5], s[4:5], 0, v[2:3]
	v_lshl_add_u64 v[4:5], v[4:5], 0, s[8:9]
	v_mfma_f32_16x16x32_bf16 v[114:117], v[142:145], v[190:193], v[114:117]
	global_load_dwordx4 v[6:9], v2, s[4:5] nt
	global_load_dwordx4 v[10:13], v[4:5], off nt
	s_mov_b32 s100, 3
	v_mfma_f32_16x16x32_bf16 v[102:105], v[150:153], v[190:193], v[102:105]
	s_mov_b32 s98, s42
	s_add_i32 s42, s42, 1
	s_add_u32 s4, s24, 0xfff80080
	s_addc_u32 s5, s25, -1
	v_mfma_f32_16x16x32_bf16 v[98:101], v[142:145], v[182:185], v[98:101]
	s_cmp_eq_u32 s60, 28
	s_cselect_b32 s5, s11, s5
	s_cselect_b32 s4, s56, s4
	s_cselect_b32 s35, s15, s59
	s_cselect_b32 s34, s57, s58
	v_mfma_f32_16x16x32_bf16 v[86:89], v[150:153], v[182:185], v[86:89]
	v_mfma_f32_16x16x32_bf16 v[82:85], v[142:145], v[174:177], v[82:85]
	v_mfma_f32_16x16x32_bf16 v[78:81], v[150:153], v[174:177], v[78:81]
	v_mfma_f32_16x16x32_bf16 v[130:133], v[146:149], v[202:205], v[130:133]
	v_mfma_f32_16x16x32_bf16 v[118:121], v[154:157], v[202:205], v[118:121]
	v_mfma_f32_16x16x32_bf16 v[114:117], v[146:149], v[194:197], v[114:117]
	v_mfma_f32_16x16x32_bf16 v[102:105], v[154:157], v[194:197], v[102:105]
	v_mfma_f32_16x16x32_bf16 v[98:101], v[146:149], v[186:189], v[98:101]
	v_mfma_f32_16x16x32_bf16 v[86:89], v[154:157], v[186:189], v[86:89]
	v_mfma_f32_16x16x32_bf16 v[82:85], v[146:149], v[178:181], v[82:85]
	v_mfma_f32_16x16x32_bf16 v[78:81], v[154:157], v[178:181], v[78:81]
	s_setprio 0
	s_branch .Lp4vg_mmjoin_a
.Lp4vg_mmslow_a:
	s_mov_b32 s100, 0
	s_cmp_lt_i32 s98, 0
	s_cbranch_scc1 .Lp4vg_nf_a
	s_add_i32 s22, s98, s47
	s_lshr_b32 s4, s22, 31
	s_add_i32 s4, s22, s4
	s_ashr_i32 s23, s4, 1
	s_ashr_i32 s4, s4, 11
	s_and_b32 s5, s23, 0x3ff
	s_ashr_i32 s34, s4, 31
	s_lshl_b32 s4, s4, 10
	v_pk_mul_f32 v[6:7], v[6:7], s[2:3] op_sel_hi:[1,0]
	v_pk_mul_f32 v[8:9], v[8:9], s[2:3] op_sel_hi:[1,0]
	v_pk_mul_f32 v[10:11], v[10:11], s[2:3] op_sel_hi:[1,0]
	v_pk_mul_f32 v[12:13], v[12:13], s[2:3] op_sel_hi:[1,0]
	s_or_b32 s4, s4, s5
	v_cvt_pk_fp8_f32 v6, v6, v10
	s_mul_hi_u32 s5, s4, 0x2100
	s_mulk_i32 s34, 0x2100
	v_cvt_pk_fp8_f32 v6, v7, v11 op_sel:[0,0,1]
	s_add_i32 s5, s5, s34
	s_mulk_i32 s4, 0x2100
	v_cvt_pk_fp8_f32 v7, v8, v12
	v_readlane_b32 s101, v251, 49
	s_add_u32 s4, s101, s4
	v_readlane_b32 s101, v251, 31
	s_addc_u32 s5, s101, s5
	v_cvt_pk_fp8_f32 v7, v9, v13 op_sel:[0,0,1]
	v_lshl_or_b32 v222, s22, 11, v208
	s_lshl_b32 s34, s23, 12
	v_subrev_u32_e32 v4, s34, v222
	v_ashrrev_i32_e32 v5, 31, v4
	v_lshl_add_u64 v[4:5], v[4:5], 1, s[4:5]
	global_store_dwordx2 v[4:5], v[6:7], off nt
	s_mov_b32 s100, 1
.Lp4vg_nf_a:
	s_mov_b32 s98, -1
	s_cmp_gt_i32 s42, 31
	s_cbranch_scc1 .Lp4vg_ni_a
	s_add_i32 s22, s42, s47
	s_lshr_b32 s4, s22, 31
	s_add_i32 s4, s22, s4
	s_ashr_i32 s23, s4, 1
	s_ashr_i32 s4, s4, 11
	s_ashr_i32 s5, s4, 31
	s_lshl_b64 s[4:5], s[4:5], 25
	v_readlane_b32 s34, v251, 36
	v_readlane_b32 s35, v251, 37
	s_add_u32 s4, s34, s4
	s_addc_u32 s5, s35, s5
	s_lshl_b32 s34, s23, 15
	s_and_b32 s34, s34, 0x1ff8000
	s_add_u32 s34, s4, s34
	s_addc_u32 s35, s5, 0
	s_lshl_b32 s4, s23, 12
	s_lshl_b32 s5, s22, 11
	s_sub_i32 s4, s5, s4
	s_ashr_i32 s5, s4, 31
	s_lshl_b64 s[4:5], s[4:5], 2
	s_add_u32 s4, s34, s4
	s_addc_u32 s5, s35, s5
	v_lshlrev_b32_e32 v2, 2, v208
	v_lshl_add_u64 v[4:5], s[4:5], 0, v[2:3]
	v_lshl_add_u64 v[4:5], v[4:5], 0, s[8:9]
	global_load_dwordx4 v[6:9], v2, s[4:5] nt
	global_load_dwordx4 v[10:13], v[4:5], off nt
	s_mov_b32 s98, s42
	s_add_i32 s42, s42, 1
	s_add_i32 s100, s100, 2
.Lp4vg_ni_a:
	s_add_u32 s4, s24, 0xfff80080
	s_addc_u32 s5, s25, -1
	s_cmp_eq_u32 s60, 28
	s_cselect_b32 s5, s11, s5
	s_cselect_b32 s4, s56, s4
	s_cselect_b32 s35, s15, s59
	s_cselect_b32 s34, s57, s58
	s_setprio 1
	s_waitcnt lgkmcnt(0)
	v_mfma_f32_16x16x32_bf16 v[138:141], v[158:161], v[198:201], v[138:141]
	v_mfma_f32_16x16x32_bf16 v[134:137], v[166:169], v[198:201], v[134:137]
	v_mfma_f32_16x16x32_bf16 v[126:129], v[158:161], v[190:193], v[126:129]
	v_mfma_f32_16x16x32_bf16 v[122:125], v[166:169], v[190:193], v[122:125]
	v_mfma_f32_16x16x32_bf16 v[110:113], v[158:161], v[182:185], v[110:113]
	v_mfma_f32_16x16x32_bf16 v[106:109], v[166:169], v[182:185], v[106:109]
	v_mfma_f32_16x16x32_bf16 v[94:97], v[158:161], v[174:177], v[94:97]
	v_mfma_f32_16x16x32_bf16 v[90:93], v[166:169], v[174:177], v[90:93]
	v_mfma_f32_16x16x32_bf16 v[138:141], v[162:165], v[202:205], v[138:141]
	v_mfma_f32_16x16x32_bf16 v[134:137], v[170:173], v[202:205], v[134:137]
	v_mfma_f32_16x16x32_bf16 v[126:129], v[162:165], v[194:197], v[126:129]
	v_mfma_f32_16x16x32_bf16 v[122:125], v[170:173], v[194:197], v[122:125]
	v_mfma_f32_16x16x32_bf16 v[110:113], v[162:165], v[186:189], v[110:113]
	v_mfma_f32_16x16x32_bf16 v[106:109], v[170:173], v[186:189], v[106:109]
	v_mfma_f32_16x16x32_bf16 v[94:97], v[162:165], v[178:181], v[94:97]
	v_mfma_f32_16x16x32_bf16 v[90:93], v[170:173], v[178:181], v[90:93]
	s_setprio 0
	s_setprio 1
	v_mfma_f32_16x16x32_bf16 v[130:133], v[142:145], v[198:201], v[130:133]
	v_mfma_f32_16x16x32_bf16 v[118:121], v[150:153], v[198:201], v[118:121]
	v_mfma_f32_16x16x32_bf16 v[114:117], v[142:145], v[190:193], v[114:117]
	v_mfma_f32_16x16x32_bf16 v[102:105], v[150:153], v[190:193], v[102:105]
	v_mfma_f32_16x16x32_bf16 v[98:101], v[142:145], v[182:185], v[98:101]
	v_mfma_f32_16x16x32_bf16 v[86:89], v[150:153], v[182:185], v[86:89]
	v_mfma_f32_16x16x32_bf16 v[82:85], v[142:145], v[174:177], v[82:85]
	v_mfma_f32_16x16x32_bf16 v[78:81], v[150:153], v[174:177], v[78:81]
	v_mfma_f32_16x16x32_bf16 v[130:133], v[146:149], v[202:205], v[130:133]
	v_mfma_f32_16x16x32_bf16 v[118:121], v[154:157], v[202:205], v[118:121]
	v_mfma_f32_16x16x32_bf16 v[114:117], v[146:149], v[194:197], v[114:117]
	v_mfma_f32_16x16x32_bf16 v[102:105], v[154:157], v[194:197], v[102:105]
	v_mfma_f32_16x16x32_bf16 v[98:101], v[146:149], v[186:189], v[98:101]
	v_mfma_f32_16x16x32_bf16 v[86:89], v[154:157], v[186:189], v[86:89]
	v_mfma_f32_16x16x32_bf16 v[82:85], v[146:149], v[178:181], v[82:85]
	v_mfma_f32_16x16x32_bf16 v[78:81], v[154:157], v[178:181], v[78:81]
	s_setprio 0
.Lp4vg_mmjoin_a:
	s_barrier
	s_mov_b32 m0, s33
	v_lshl_add_u64 v[4:5], s[34:35], 0, v[210:211]
	s_add_u32 s64, s34, 0x80000
	ds_read_b128 v[174:177], v230 offset:16384
	ds_read_b128 v[178:181], v230 offset:17408
	ds_read_b128 v[182:185], v230 offset:18432
	ds_read_b128 v[186:189], v230 offset:19456
	ds_read_b128 v[190:193], v230 offset:20480
	ds_read_b128 v[194:197], v230 offset:21504
	ds_read_b128 v[198:201], v230 offset:22528
	ds_read_b128 v[202:205], v230 offset:23552
	global_load_lds_dwordx4 v[4:5], off
	v_lshl_add_u64 v[222:223], s[34:35], 0, v[212:213]
	s_mov_b32 m0, s36
	s_addc_u32 s65, s35, 0
	global_load_lds_dwordx4 v[222:223], off
	v_lshl_add_u64 v[224:225], s[64:65], 0, v[210:211]
	s_mov_b32 m0, s37
	v_lshl_add_u64 v[226:227], s[4:5], 0, v[212:213]
	global_load_lds_dwordx4 v[224:225], off
	v_lshl_add_u64 v[224:225], s[64:65], 0, v[212:213]
	s_mov_b32 m0, s41
	s_nop 0
	global_load_lds_dwordx4 v[224:225], off
	v_lshl_add_u64 v[224:225], s[4:5], 0, v[210:211]
	s_mov_b32 m0, s21
	s_nop 0
	global_load_lds_dwordx4 v[224:225], off
	s_mov_b32 m0, s43
	s_nop 0
	global_load_lds_dwordx4 v[226:227], off
	s_cmp_eq_u32 s100, 3
	s_cbranch_scc1 .Lp4vg_w11_a2
	s_waitcnt vmcnt(8)
	s_branch .Lp4vg_wd_a2

.Lp4vg_wd_a2:
	s_waitcnt lgkmcnt(0)
	s_barrier
	s_setprio 1
	s_waitcnt lgkmcnt(0)
	v_mfma_f32_16x16x32_bf16 v[74:77], v[158:161], v[174:177], v[74:77]
	v_mfma_f32_16x16x32_bf16 v[70:73], v[166:169], v[174:177], v[70:73]
	v_mfma_f32_16x16x32_bf16 v[62:65], v[158:161], v[182:185], v[62:65]
	v_mfma_f32_16x16x32_bf16 v[58:61], v[166:169], v[182:185], v[58:61]
	v_mfma_f32_16x16x32_bf16 v[46:49], v[158:161], v[190:193], v[46:49]
	v_mfma_f32_16x16x32_bf16 v[42:45], v[166:169], v[190:193], v[42:45]
	v_mfma_f32_16x16x32_bf16 v[30:33], v[158:161], v[198:201], v[30:33]
	v_mfma_f32_16x16x32_bf16 v[26:29], v[166:169], v[198:201], v[26:29]
	v_mfma_f32_16x16x32_bf16 v[74:77], v[162:165], v[178:181], v[74:77]
	v_mfma_f32_16x16x32_bf16 v[70:73], v[170:173], v[178:181], v[70:73]
	v_mfma_f32_16x16x32_bf16 v[62:65], v[162:165], v[186:189], v[62:65]
	v_mfma_f32_16x16x32_bf16 v[58:61], v[170:173], v[186:189], v[58:61]
	v_mfma_f32_16x16x32_bf16 v[46:49], v[162:165], v[194:197], v[46:49]
	v_mfma_f32_16x16x32_bf16 v[42:45], v[170:173], v[194:197], v[42:45]
	v_mfma_f32_16x16x32_bf16 v[30:33], v[162:165], v[202:205], v[30:33]
	v_mfma_f32_16x16x32_bf16 v[26:29], v[170:173], v[202:205], v[26:29]
	s_setprio 0
	s_setprio 1
	v_mfma_f32_16x16x32_bf16 v[66:69], v[142:145], v[174:177], v[66:69]
	v_mfma_f32_16x16x32_bf16 v[54:57], v[150:153], v[174:177], v[54:57]
	v_mfma_f32_16x16x32_bf16 v[50:53], v[142:145], v[182:185], v[50:53]
	v_mfma_f32_16x16x32_bf16 v[38:41], v[150:153], v[182:185], v[38:41]
	v_mfma_f32_16x16x32_bf16 v[34:37], v[142:145], v[190:193], v[34:37]
	v_mfma_f32_16x16x32_bf16 v[22:25], v[150:153], v[190:193], v[22:25]
	v_mfma_f32_16x16x32_bf16 v[18:21], v[142:145], v[198:201], v[18:21]
	v_mfma_f32_16x16x32_bf16 v[14:17], v[150:153], v[198:201], v[14:17]
	v_mfma_f32_16x16x32_bf16 v[66:69], v[146:149], v[178:181], v[66:69]
	v_mfma_f32_16x16x32_bf16 v[54:57], v[154:157], v[178:181], v[54:57]
	v_mfma_f32_16x16x32_bf16 v[50:53], v[146:149], v[186:189], v[50:53]
	v_mfma_f32_16x16x32_bf16 v[38:41], v[154:157], v[186:189], v[38:41]
	v_mfma_f32_16x16x32_bf16 v[34:37], v[146:149], v[194:197], v[34:37]
	v_mfma_f32_16x16x32_bf16 v[22:25], v[154:157], v[194:197], v[22:25]
	v_mfma_f32_16x16x32_bf16 v[18:21], v[146:149], v[202:205], v[18:21]
	v_mfma_f32_16x16x32_bf16 v[14:17], v[154:157], v[202:205], v[14:17]
	s_setprio 0
	s_barrier
	v_add_u32_e32 v2, 0x18000, v1
	ds_read_b128 v[158:161], v2
	ds_read_b128 v[162:165], v2 offset:1024
	ds_read_b128 v[166:169], v2 offset:2048
	ds_read_b128 v[170:173], v2 offset:3072
	v_add_u32_e32 v2, 0x1c000, v1
	ds_read_b128 v[142:145], v2
	ds_read_b128 v[146:149], v2 offset:1024
	ds_read_b128 v[150:153], v2 offset:2048
	ds_read_b128 v[154:157], v2 offset:3072
	s_add_u32 s4, s4, 0x80000
	s_addc_u32 s5, s5, 0
	s_mov_b32 m0, s44
	v_lshl_add_u64 v[232:233], s[4:5], 0, v[210:211]
	ds_read_b128 v[198:201], v230 offset:32768
	ds_read_b128 v[202:205], v230 offset:33792
	ds_read_b128 v[190:193], v230 offset:34816
	ds_read_b128 v[194:197], v230 offset:35840
	ds_read_b128 v[182:185], v230 offset:36864
	ds_read_b128 v[186:189], v230 offset:37888
	ds_read_b128 v[174:177], v230 offset:38912
	ds_read_b128 v[178:181], v230 offset:39936
	global_load_lds_dwordx4 v[232:233], off
	v_lshl_add_u64 v[232:233], s[4:5], 0, v[212:213]
	s_mov_b32 m0, s46
	s_nop 0
	global_load_lds_dwordx4 v[232:233], off
	s_cmp_eq_u32 s100, 3
	s_cbranch_scc1 .Lp4vg_w11_b1
	s_waitcnt vmcnt(8)
	s_branch .Lp4vg_wd_b1

;     __device__ __forceinline__ void finish(v4i_t& t0, v4i_t& t1, int j, int tid) const {
;         asm volatile("" : "+v"(t0), "+v"(t1));
;         const float* s0; unsigned char* d; addr(j, tid, s0, d);
;         const f32x4 r0 = __builtin_bit_cast(f32x4, t0) * 64.f, r1 = __builtin_bit_cast(f32x4, t1) * 64.f;
;         int w0 = 0, w1 = 0; w0 = __builtin_amdgcn_cvt_pk_fp8_f32(r0[0], r1[0], w0, false); w0 = __builtin_amdgcn_cvt_pk_fp8_f32(r0[1], r1[1], w0, true);
;         w1 = __builtin_amdgcn_cvt_pk_fp8_f32(r0[2], r1[2], w1, false); w1 = __builtin_amdgcn_cvt_pk_fp8_f32(r0[3], r1[3], w1, true);
;         typedef int v2is __attribute__((ext_vector_type(2))); __builtin_nontemporal_store((v2is){w0, w1}, (v2is*)d);
.Lp4vg_wd_b1:
	s_waitcnt lgkmcnt(0)
	s_cmp_lt_i32 s99, 0
	s_cbranch_scc1 .Lp4vg_mmslow_b
	s_cmp_gt_i32 s42, 31
	s_cbranch_scc1 .Lp4vg_mmslow_b
	s_barrier
	s_setprio 1
	s_waitcnt lgkmcnt(0)
	v_mfma_f32_16x16x32_bf16 v[138:141], v[158:161], v[198:201], v[138:141]
	s_add_i32 s22, s99, s47
	s_lshr_b32 s4, s22, 31
	s_add_i32 s4, s22, s4
	v_mfma_f32_16x16x32_bf16 v[134:137], v[166:169], v[198:201], v[134:137]
	s_ashr_i32 s23, s4, 1
	s_ashr_i32 s4, s4, 11
	s_and_b32 s5, s23, 0x3ff
	v_mfma_f32_16x16x32_bf16 v[126:129], v[158:161], v[190:193], v[126:129]
	s_ashr_i32 s61, s4, 31
	s_lshl_b32 s4, s4, 10
	v_pk_mul_f32 v[242:243], v[242:243], s[2:3] op_sel_hi:[1,0]
	v_mfma_f32_16x16x32_bf16 v[122:125], v[166:169], v[190:193], v[122:125]
	v_pk_mul_f32 v[244:245], v[244:245], s[2:3] op_sel_hi:[1,0]
	v_pk_mul_f32 v[246:247], v[246:247], s[2:3] op_sel_hi:[1,0]
	v_pk_mul_f32 v[248:249], v[248:249], s[2:3] op_sel_hi:[1,0]
	v_mfma_f32_16x16x32_bf16 v[110:113], v[158:161], v[182:185], v[110:113]
	s_or_b32 s4, s4, s5
	v_cvt_pk_fp8_f32 v242, v242, v246
	s_mul_hi_u32 s5, s4, 0x2100
	v_mfma_f32_16x16x32_bf16 v[106:109], v[166:169], v[182:185], v[106:109]
	s_mulk_i32 s61, 0x2100
	v_cvt_pk_fp8_f32 v242, v243, v247 op_sel:[0,0,1]
	s_add_i32 s5, s5, s61
	v_mfma_f32_16x16x32_bf16 v[94:97], v[158:161], v[174:177], v[94:97]
	s_mulk_i32 s4, 0x2100
	v_cvt_pk_fp8_f32 v243, v244, v248
	v_readlane_b32 s101, v251, 49
	v_mfma_f32_16x16x32_bf16 v[90:93], v[166:169], v[174:177], v[90:93]
	s_add_u32 s4, s101, s4
	v_readlane_b32 s101, v251, 31
	s_addc_u32 s5, s101, s5
	v_mfma_f32_16x16x32_bf16 v[138:141], v[162:165], v[202:205], v[138:141]
	v_cvt_pk_fp8_f32 v243, v245, v249 op_sel:[0,0,1]
	v_lshl_or_b32 v234, s22, 11, v208
	s_lshl_b32 s61, s23, 12
	v_mfma_f32_16x16x32_bf16 v[134:137], v[170:173], v[202:205], v[134:137]
	v_subrev_u32_e32 v232, s61, v234
	v_ashrrev_i32_e32 v233, 31, v232
	v_lshl_add_u64 v[232:233], v[232:233], 1, s[4:5]
	v_mfma_f32_16x16x32_bf16 v[126:129], v[162:165], v[194:197], v[126:129]
	global_store_dwordx2 v[232:233], v[242:243], off nt
	s_add_i32 s22, s42, s47
	s_lshr_b32 s4, s22, 31
	v_mfma_f32_16x16x32_bf16 v[122:125], v[170:173], v[194:197], v[122:125]
	s_add_i32 s4, s22, s4
	s_ashr_i32 s23, s4, 1
	s_ashr_i32 s4, s4, 11
	v_mfma_f32_16x16x32_bf16 v[110:113], v[162:165], v[186:189], v[110:113]
	s_ashr_i32 s5, s4, 31
	s_lshl_b64 s[4:5], s[4:5], 25
	v_readlane_b32 s64, v251, 36
	v_mfma_f32_16x16x32_bf16 v[106:109], v[170:173], v[186:189], v[106:109]
	v_readlane_b32 s65, v251, 37
	s_add_u32 s4, s64, s4
	s_addc_u32 s5, s65, s5
	v_mfma_f32_16x16x32_bf16 v[94:97], v[162:165], v[178:181], v[94:97]
	s_lshl_b32 s64, s23, 15
	s_and_b32 s64, s64, 0x1ff8000
	s_add_u32 s64, s4, s64
	s_addc_u32 s65, s5, 0
	v_mfma_f32_16x16x32_bf16 v[90:93], v[170:173], v[178:181], v[90:93]
	s_setprio 0
	s_setprio 1
	s_lshl_b32 s4, s23, 12
	s_lshl_b32 s5, s22, 11
	s_sub_i32 s4, s5, s4
	v_mfma_f32_16x16x32_bf16 v[130:133], v[142:145], v[198:201], v[130:133]
	s_ashr_i32 s5, s4, 31
	s_lshl_b64 s[4:5], s[4:5], 2
	s_add_u32 s4, s64, s4
	s_addc_u32 s5, s65, s5
	v_mfma_f32_16x16x32_bf16 v[118:121], v[150:153], v[198:201], v[118:121]
	v_lshlrev_b32_e32 v2, 2, v208
	v_lshl_add_u64 v[232:233], s[4:5], 0, v[2:3]
	v_lshl_add_u64 v[232:233], v[232:233], 0, s[8:9]
	v_mfma_f32_16x16x32_bf16 v[114:117], v[142:145], v[190:193], v[114:117]
	global_load_dwordx4 v[242:245], v2, s[4:5] nt
	global_load_dwordx4 v[246:249], v[232:233], off nt
	s_mov_b32 s100, 3
	v_mfma_f32_16x16x32_bf16 v[102:105], v[150:153], v[190:193], v[102:105]
	s_mov_b32 s99, s42
	s_add_i32 s42, s42, 1
	v_mfma_f32_16x16x32_bf16 v[98:101], v[142:145], v[182:185], v[98:101]
	v_mfma_f32_16x16x32_bf16 v[86:89], v[150:153], v[182:185], v[86:89]
	v_mfma_f32_16x16x32_bf16 v[82:85], v[142:145], v[174:177], v[82:85]
	v_mfma_f32_16x16x32_bf16 v[78:81], v[150:153], v[174:177], v[78:81]
	v_mfma_f32_16x16x32_bf16 v[130:133], v[146:149], v[202:205], v[130:133]
	v_mfma_f32_16x16x32_bf16 v[118:121], v[154:157], v[202:205], v[118:121]
	v_mfma_f32_16x16x32_bf16 v[114:117], v[146:149], v[194:197], v[114:117]
	v_mfma_f32_16x16x32_bf16 v[102:105], v[154:157], v[194:197], v[102:105]
	v_mfma_f32_16x16x32_bf16 v[98:101], v[146:149], v[186:189], v[98:101]
	v_mfma_f32_16x16x32_bf16 v[86:89], v[154:157], v[186:189], v[86:89]
	v_mfma_f32_16x16x32_bf16 v[82:85], v[146:149], v[178:181], v[82:85]
	v_mfma_f32_16x16x32_bf16 v[78:81], v[154:157], v[178:181], v[78:81]
	s_setprio 0
	s_branch .Lp4vg_mmafter_b
.Lp4vg_mmslow_b:
	s_mov_b32 s100, 0
	s_cmp_lt_i32 s99, 0
	s_cbranch_scc1 .Lp4vg_nf_b
	s_add_i32 s22, s99, s47
	s_lshr_b32 s4, s22, 31
	s_add_i32 s4, s22, s4
	s_ashr_i32 s23, s4, 1
	s_ashr_i32 s4, s4, 11
	s_and_b32 s5, s23, 0x3ff
	s_ashr_i32 s61, s4, 31
	s_lshl_b32 s4, s4, 10
	v_pk_mul_f32 v[242:243], v[242:243], s[2:3] op_sel_hi:[1,0]
	v_pk_mul_f32 v[244:245], v[244:245], s[2:3] op_sel_hi:[1,0]
	v_pk_mul_f32 v[246:247], v[246:247], s[2:3] op_sel_hi:[1,0]
	v_pk_mul_f32 v[248:249], v[248:249], s[2:3] op_sel_hi:[1,0]
	s_or_b32 s4, s4, s5
	v_cvt_pk_fp8_f32 v242, v242, v246
	s_mul_hi_u32 s5, s4, 0x2100
	s_mulk_i32 s61, 0x2100
	v_cvt_pk_fp8_f32 v242, v243, v247 op_sel:[0,0,1]
	s_add_i32 s5, s5, s61
	s_mulk_i32 s4, 0x2100
	v_cvt_pk_fp8_f32 v243, v244, v248
	v_readlane_b32 s101, v251, 49
	s_add_u32 s4, s101, s4
	v_readlane_b32 s101, v251, 31
	s_addc_u32 s5, s101, s5
	v_cvt_pk_fp8_f32 v243, v245, v249 op_sel:[0,0,1]
	v_lshl_or_b32 v234, s22, 11, v208
	s_lshl_b32 s61, s23, 12
	v_subrev_u32_e32 v232, s61, v234
	v_ashrrev_i32_e32 v233, 31, v232
	v_lshl_add_u64 v[232:233], v[232:233], 1, s[4:5]
	global_store_dwordx2 v[232:233], v[242:243], off nt
	s_mov_b32 s100, 1
.Lp4vg_nf_b:
	s_mov_b32 s99, -1
	s_cmp_gt_i32 s42, 31
	s_cbranch_scc1 .Lp4vg_ni_b
	s_add_i32 s22, s42, s47
	s_lshr_b32 s4, s22, 31
	s_add_i32 s4, s22, s4
	s_ashr_i32 s23, s4, 1
	s_ashr_i32 s4, s4, 11
	s_ashr_i32 s5, s4, 31
	s_lshl_b64 s[4:5], s[4:5], 25
	v_readlane_b32 s64, v251, 36
	v_readlane_b32 s65, v251, 37
	s_add_u32 s4, s64, s4
	s_addc_u32 s5, s65, s5
	s_lshl_b32 s64, s23, 15
	s_and_b32 s64, s64, 0x1ff8000
	s_add_u32 s64, s4, s64
	s_addc_u32 s65, s5, 0
	s_lshl_b32 s4, s23, 12
	s_lshl_b32 s5, s22, 11
	s_sub_i32 s4, s5, s4
	s_ashr_i32 s5, s4, 31
	s_lshl_b64 s[4:5], s[4:5], 2
	s_add_u32 s4, s64, s4
	s_addc_u32 s5, s65, s5
	v_lshlrev_b32_e32 v2, 2, v208
	v_lshl_add_u64 v[232:233], s[4:5], 0, v[2:3]
	v_lshl_add_u64 v[232:233], v[232:233], 0, s[8:9]
	global_load_dwordx4 v[242:245], v2, s[4:5] nt
	global_load_dwordx4 v[246:249], v[232:233], off nt
	s_mov_b32 s99, s42
	s_add_i32 s42, s42, 1
	s_add_i32 s100, s100, 2

;     __device__ __forceinline__ void operator()(const f32x4 (&acc)[2][2][4][2], const Unit& u, int wr, int wc, int fr, int fq) const {
;         const int row0 = u.pm * BM + wr * 64 + fr, col0 = u.cn * BM + wc * 32 + 4 * fq;
; #pragma unroll
;         for (int ai = 0; ai < 2; ++ai)
; #pragma unroll
;             for (int m = 0; m < 4; ++m) { const size_t off = (size_t)(row0 + ai * HALF + m * 16) * ldc + col0;
; #pragma unroll
;                 for (int bj = 0; bj < 2; ++bj)
; #pragma unroll
;                     for (int n = 0; n < 2; ++n) { const f32x4 b = *(const f32x4*)(base + off + bj * HALF + n * 16); *(f32x4*)(out + off + bj * HALF + n * 16) = acc[ai][bj][m][n] + b; } }
;     }
.LBB0_548:
	v_mov_b32_e32 v2, v0
	s_lshl_b32 s5, s20, 8
	v_readfirstlane_b32 s4, v2
	s_ashr_i32 s11, s4, 2
	s_andn2_b32 s11, s11, 63
	s_lshr_b32 s4, s4, 1
	s_add_i32 s11, s11, s5
	s_lshl_b32 s5, s55, 8
	s_and_b32 s4, s4, 0x60
	v_and_or_b32 v146, v2, 15, s11
	s_or_b32 s4, s4, s5
	v_lshrrev_b32_e32 v2, 2, v2
	v_and_or_b32 v148, v2, 12, s4
	v_ashrrev_i32_e32 v147, 31, v146
	v_ashrrev_i32_e32 v149, 31, v148
	v_lshlrev_b64 v[4:5], 11, v[146:147]
	v_lshl_add_u64 v[4:5], v[4:5], 0, v[148:149]
	v_readlane_b32 s56, v251, 3
	v_lshlrev_b64 v[4:5], 2, v[4:5]
	v_readlane_b32 s57, v251, 4
	v_readlane_b32 s12, v251, 52
	v_readlane_b32 s13, v251, 53
	v_lshl_add_u64 v[150:151], s[56:57], 0, v[4:5]
	v_lshl_add_u64 v[152:153], s[12:13], 0, v[4:5]
	s_mov_b64 s[4:5], 0x100000
	s_and_b64 vcc, exec, s[6:7]
	v_readlane_b32 s58, v251, 5
	v_readlane_b32 s59, v251, 6
	v_readlane_b32 s60, v251, 7
	v_readlane_b32 s61, v251, 8
	v_readlane_b32 s62, v251, 9
	v_readlane_b32 s63, v251, 10
	v_readlane_b32 s64, v251, 11
	v_readlane_b32 s65, v251, 12
	v_readlane_b32 s66, v251, 13
	v_readlane_b32 s67, v251, 14
	v_readlane_b32 s68, v251, 15
	v_readlane_b32 s69, v251, 16
	v_readlane_b32 s70, v251, 17
	v_readlane_b32 s71, v251, 18
	s_add_u32 s4, s56, 0x0
	s_addc_u32 s5, s57, 0
	global_load_dwordx4 v[142:145], v4, s[4:5]
	global_load_dwordx4 v[146:149], v4, s[4:5] offset:64
	global_load_dwordx4 v[150:153], v4, s[4:5] offset:512
	global_load_dwordx4 v[154:157], v4, s[4:5] offset:576
	s_add_u32 s4, s56, 0x20000
	s_addc_u32 s5, s57, 0
	global_load_dwordx4 v[158:161], v4, s[4:5]
	global_load_dwordx4 v[162:165], v4, s[4:5] offset:64
	global_load_dwordx4 v[166:169], v4, s[4:5] offset:512
	global_load_dwordx4 v[170:173], v4, s[4:5] offset:576
	s_add_u32 s4, s56, 0x40000
	s_addc_u32 s5, s57, 0
	global_load_dwordx4 v[174:177], v4, s[4:5]
	global_load_dwordx4 v[178:181], v4, s[4:5] offset:64
	global_load_dwordx4 v[182:185], v4, s[4:5] offset:512
	global_load_dwordx4 v[186:189], v4, s[4:5] offset:576
	s_add_u32 s4, s56, 0x60000
	s_addc_u32 s5, s57, 0
	global_load_dwordx4 v[190:193], v4, s[4:5]
	global_load_dwordx4 v[194:197], v4, s[4:5] offset:64
	global_load_dwordx4 v[198:201], v4, s[4:5] offset:512
	global_load_dwordx4 v[202:205], v4, s[4:5] offset:576
	s_add_u32 s100, s12, 0x0
	s_addc_u32 s101, s13, 0
	s_add_u32 s4, s56, 0x100000
	s_addc_u32 s5, s57, 0
	s_waitcnt vmcnt(15)
	v_pk_add_f32 v[142:143], v[138:139], v[142:143]
	v_pk_add_f32 v[144:145], v[140:141], v[144:145]
	global_store_dwordx4 v4, v[142:145], s[100:101]
	global_load_dwordx4 v[138:141], v4, s[4:5]
	s_waitcnt vmcnt(16)
	v_pk_add_f32 v[146:147], v[134:135], v[146:147]
	v_pk_add_f32 v[148:149], v[136:137], v[148:149]
	global_store_dwordx4 v4, v[146:149], s[100:101] offset:64
	global_load_dwordx4 v[134:137], v4, s[4:5] offset:64
	s_waitcnt vmcnt(17)
	v_pk_add_f32 v[150:151], v[130:131], v[150:151]
	v_pk_add_f32 v[152:153], v[132:133], v[152:153]
	global_store_dwordx4 v4, v[150:153], s[100:101] offset:512
	global_load_dwordx4 v[130:133], v4, s[4:5] offset:512
	s_waitcnt vmcnt(18)
	v_pk_add_f32 v[154:155], v[118:119], v[154:155]
	v_pk_add_f32 v[156:157], v[120:121], v[156:157]
	global_store_dwordx4 v4, v[154:157], s[100:101] offset:576
	global_load_dwordx4 v[118:121], v4, s[4:5] offset:576
	s_add_u32 s100, s12, 0x20000
	s_addc_u32 s101, s13, 0
	s_add_u32 s4, s56, 0x120000
	s_addc_u32 s5, s57, 0
	s_waitcnt vmcnt(19)
	v_pk_add_f32 v[158:159], v[126:127], v[158:159]
	v_pk_add_f32 v[160:161], v[128:129], v[160:161]
	global_store_dwordx4 v4, v[158:161], s[100:101]
	global_load_dwordx4 v[126:129], v4, s[4:5]
	s_waitcnt vmcnt(20)
	v_pk_add_f32 v[162:163], v[122:123], v[162:163]
	v_pk_add_f32 v[164:165], v[124:125], v[164:165]
	global_store_dwordx4 v4, v[162:165], s[100:101] offset:64
	global_load_dwordx4 v[122:125], v4, s[4:5] offset:64
	s_waitcnt vmcnt(21)
	v_pk_add_f32 v[166:167], v[114:115], v[166:167]
	v_pk_add_f32 v[168:169], v[116:117], v[168:169]
	global_store_dwordx4 v4, v[166:169], s[100:101] offset:512
	global_load_dwordx4 v[114:117], v4, s[4:5] offset:512
	s_waitcnt vmcnt(22)
	v_pk_add_f32 v[170:171], v[102:103], v[170:171]
	v_pk_add_f32 v[172:173], v[104:105], v[172:173]
	global_store_dwordx4 v4, v[170:173], s[100:101] offset:576
	global_load_dwordx4 v[102:105], v4, s[4:5] offset:576
	s_add_u32 s100, s12, 0x40000
	s_addc_u32 s101, s13, 0
	s_add_u32 s4, s56, 0x140000
	s_addc_u32 s5, s57, 0
	s_waitcnt vmcnt(23)
	v_pk_add_f32 v[174:175], v[110:111], v[174:175]
	v_pk_add_f32 v[176:177], v[112:113], v[176:177]
	global_store_dwordx4 v4, v[174:177], s[100:101]
	global_load_dwordx4 v[110:113], v4, s[4:5]
	s_waitcnt vmcnt(24)
;     __device__ __forceinline__ void operator()(const f32x4 (&acc)[2][2][4][2], const Unit& u, int wr, int wc, int fr, int fq) const {
;         const int row0 = u.pm * BM + wr * 64 + fr, col0 = u.cn * BM + wc * 32 + 4 * fq;
; #pragma unroll
;         for (int ai = 0; ai < 2; ++ai)
; #pragma unroll
;             for (int m = 0; m < 4; ++m) { const size_t off = (size_t)(row0 + ai * HALF + m * 16) * ldc + col0;
; #pragma unroll
;                 for (int bj = 0; bj < 2; ++bj)
; #pragma unroll
;                     for (int n = 0; n < 2; ++n) { const f32x4 b = *(const f32x4*)(base + off + bj * HALF + n * 16); *(f32x4*)(out + off + bj * HALF + n * 16) = acc[ai][bj][m][n] + b; } }
;     }
	v_pk_add_f32 v[178:179], v[106:107], v[178:179]
	v_pk_add_f32 v[180:181], v[108:109], v[180:181]
	global_store_dwordx4 v4, v[178:181], s[100:101] offset:64
	global_load_dwordx4 v[106:109], v4, s[4:5] offset:64
	s_waitcnt vmcnt(25)
	v_pk_add_f32 v[182:183], v[98:99], v[182:183]
	v_pk_add_f32 v[184:185], v[100:101], v[184:185]
	global_store_dwordx4 v4, v[182:185], s[100:101] offset:512
	global_load_dwordx4 v[98:101], v4, s[4:5] offset:512
	s_waitcnt vmcnt(26)
	v_pk_add_f32 v[186:187], v[86:87], v[186:187]
	v_pk_add_f32 v[188:189], v[88:89], v[188:189]
	global_store_dwordx4 v4, v[186:189], s[100:101] offset:576
	global_load_dwordx4 v[86:89], v4, s[4:5] offset:576
	s_add_u32 s100, s12, 0x60000
	s_addc_u32 s101, s13, 0
	s_add_u32 s4, s56, 0x160000
	s_addc_u32 s5, s57, 0
	s_waitcnt vmcnt(27)
	v_pk_add_f32 v[190:191], v[94:95], v[190:191]
	v_pk_add_f32 v[192:193], v[96:97], v[192:193]
	global_store_dwordx4 v4, v[190:193], s[100:101]
	global_load_dwordx4 v[94:97], v4, s[4:5]
	s_waitcnt vmcnt(28)
	v_pk_add_f32 v[194:195], v[90:91], v[194:195]
	v_pk_add_f32 v[196:197], v[92:93], v[196:197]
	global_store_dwordx4 v4, v[194:197], s[100:101] offset:64
	global_load_dwordx4 v[90:93], v4, s[4:5] offset:64
	s_waitcnt vmcnt(29)
	v_pk_add_f32 v[198:199], v[82:83], v[198:199]
	v_pk_add_f32 v[200:201], v[84:85], v[200:201]
	global_store_dwordx4 v4, v[198:201], s[100:101] offset:512
	global_load_dwordx4 v[82:85], v4, s[4:5] offset:512
	s_waitcnt vmcnt(30)
	v_pk_add_f32 v[202:203], v[78:79], v[202:203]
	v_pk_add_f32 v[204:205], v[80:81], v[204:205]
	global_store_dwordx4 v4, v[202:205], s[100:101] offset:576
	global_load_dwordx4 v[78:81], v4, s[4:5] offset:576
	s_add_u32 s100, s12, 0x100000
	s_addc_u32 s101, s13, 0
	s_waitcnt vmcnt(30)
	v_pk_add_f32 v[138:139], v[74:75], v[138:139]
	v_pk_add_f32 v[140:141], v[76:77], v[140:141]
	global_store_dwordx4 v4, v[138:141], s[100:101]
	s_waitcnt vmcnt(29)
	v_pk_add_f32 v[134:135], v[70:71], v[134:135]
	v_pk_add_f32 v[136:137], v[72:73], v[136:137]
	global_store_dwordx4 v4, v[134:137], s[100:101] offset:64
	s_waitcnt vmcnt(28)
	v_pk_add_f32 v[130:131], v[66:67], v[130:131]
	v_pk_add_f32 v[132:133], v[68:69], v[132:133]
	global_store_dwordx4 v4, v[130:133], s[100:101] offset:512
	s_waitcnt vmcnt(27)
	v_pk_add_f32 v[118:119], v[54:55], v[118:119]
	v_pk_add_f32 v[120:121], v[56:57], v[120:121]
	global_store_dwordx4 v4, v[118:121], s[100:101] offset:576
	s_add_u32 s100, s12, 0x120000
	s_addc_u32 s101, s13, 0
	s_waitcnt vmcnt(26)
	v_pk_add_f32 v[126:127], v[62:63], v[126:127]
	v_pk_add_f32 v[128:129], v[64:65], v[128:129]
	global_store_dwordx4 v4, v[126:129], s[100:101]
	s_waitcnt vmcnt(25)
	v_pk_add_f32 v[122:123], v[58:59], v[122:123]
	v_pk_add_f32 v[124:125], v[60:61], v[124:125]
	global_store_dwordx4 v4, v[122:125], s[100:101] offset:64
	s_waitcnt vmcnt(24)
	v_pk_add_f32 v[114:115], v[50:51], v[114:115]
	v_pk_add_f32 v[116:117], v[52:53], v[116:117]
	global_store_dwordx4 v4, v[114:117], s[100:101] offset:512
	s_waitcnt vmcnt(23)
	v_pk_add_f32 v[102:103], v[38:39], v[102:103]
	v_pk_add_f32 v[104:105], v[40:41], v[104:105]
	global_store_dwordx4 v4, v[102:105], s[100:101] offset:576
	s_add_u32 s100, s12, 0x140000
	s_addc_u32 s101, s13, 0
	s_waitcnt vmcnt(22)
	v_pk_add_f32 v[110:111], v[46:47], v[110:111]
	v_pk_add_f32 v[112:113], v[48:49], v[112:113]
	global_store_dwordx4 v4, v[110:113], s[100:101]
	s_waitcnt vmcnt(21)
	v_pk_add_f32 v[106:107], v[42:43], v[106:107]
	v_pk_add_f32 v[108:109], v[44:45], v[108:109]
	global_store_dwordx4 v4, v[106:109], s[100:101] offset:64
	s_waitcnt vmcnt(20)
	v_pk_add_f32 v[98:99], v[34:35], v[98:99]
	v_pk_add_f32 v[100:101], v[36:37], v[100:101]
	global_store_dwordx4 v4, v[98:101], s[100:101] offset:512
	s_waitcnt vmcnt(19)
	v_pk_add_f32 v[86:87], v[22:23], v[86:87]
	v_pk_add_f32 v[88:89], v[24:25], v[88:89]
	global_store_dwordx4 v4, v[86:89], s[100:101] offset:576
	s_add_u32 s100, s12, 0x160000
	s_addc_u32 s101, s13, 0
	s_waitcnt vmcnt(18)
	v_pk_add_f32 v[94:95], v[30:31], v[94:95]
	v_pk_add_f32 v[96:97], v[32:33], v[96:97]
	global_store_dwordx4 v4, v[94:97], s[100:101]
	s_waitcnt vmcnt(17)
	v_pk_add_f32 v[90:91], v[26:27], v[90:91]
	v_pk_add_f32 v[92:93], v[28:29], v[92:93]
	global_store_dwordx4 v4, v[90:93], s[100:101] offset:64
	s_waitcnt vmcnt(16)
	v_pk_add_f32 v[82:83], v[18:19], v[82:83]
	v_pk_add_f32 v[84:85], v[20:21], v[84:85]
	global_store_dwordx4 v4, v[82:85], s[100:101] offset:512
	s_waitcnt vmcnt(15)
	v_pk_add_f32 v[78:79], v[14:15], v[78:79]
	v_pk_add_f32 v[80:81], v[16:17], v[80:81]
	global_store_dwordx4 v4, v[78:81], s[100:101] offset:576
	s_cbranch_vccnz .LBB0_550
	s_mov_b32 s20, s10
	s_mov_b32 s55, s14
	s_mov_b64 s[4:5], s[18:19]
	s_mov_b64 s[24:25], s[16:17]
	s_branch .LBB0_528

;     __device__ __forceinline__ void finish(v4i_t& t0, v4i_t& t1, int j, int tid) const {
;         asm volatile("" : "+v"(t0), "+v"(t1));
;         const float* s0; unsigned char* d; addr(j, tid, s0, d);
;         const f32x4 r0 = __builtin_bit_cast(f32x4, t0) * 64.f, r1 = __builtin_bit_cast(f32x4, t1) * 64.f;
;         int w0 = 0, w1 = 0; w0 = __builtin_amdgcn_cvt_pk_fp8_f32(r0[0], r1[0], w0, false); w0 = __builtin_amdgcn_cvt_pk_fp8_f32(r0[1], r1[1], w0, true);
;         w1 = __builtin_amdgcn_cvt_pk_fp8_f32(r0[2], r1[2], w1, false); w1 = __builtin_amdgcn_cvt_pk_fp8_f32(r0[3], r1[3], w1, true);
;         typedef int v2is __attribute__((ext_vector_type(2))); __builtin_nontemporal_store((v2is){w0, w1}, (v2is*)d);
;     }
.LBB0_552:
	s_barrier
	s_mov_b32 s2, 0x42800000
	s_cmp_lt_i32 s98, 0
	s_cbranch_scc1 .Lp4vg_dx
	s_add_i32 s4, s98, s47
	s_lshr_b32 s0, s4, 31
	s_add_i32 s0, s4, s0
	s_ashr_i32 s101, s0, 1
	s_ashr_i32 s0, s0, 11
	s_and_b32 s1, s101, 0x3ff
	s_ashr_i32 s3, s0, 31
	s_lshl_b32 s0, s0, 10
	v_pk_mul_f32 v[6:7], v[6:7], s[2:3] op_sel_hi:[1,0]
	v_pk_mul_f32 v[8:9], v[8:9], s[2:3] op_sel_hi:[1,0]
	v_pk_mul_f32 v[10:11], v[10:11], s[2:3] op_sel_hi:[1,0]
	v_pk_mul_f32 v[12:13], v[12:13], s[2:3] op_sel_hi:[1,0]
	s_or_b32 s0, s0, s1
	v_cvt_pk_fp8_f32 v6, v6, v10
	s_mul_hi_u32 s1, s0, 0x2100
	s_mulk_i32 s3, 0x2100
	v_cvt_pk_fp8_f32 v6, v7, v11 op_sel:[0,0,1]
	s_add_i32 s1, s1, s3
	s_mulk_i32 s0, 0x2100
	v_cvt_pk_fp8_f32 v7, v8, v12
	v_readlane_b32 s100, v251, 49
	s_add_u32 s0, s100, s0
	v_readlane_b32 s100, v251, 31
	s_addc_u32 s1, s100, s1
	v_cvt_pk_fp8_f32 v7, v9, v13 op_sel:[0,0,1]
	v_lshl_or_b32 v14, s4, 11, v208
	s_lshl_b32 s3, s101, 12
	v_subrev_u32_e32 v2, s3, v14
	v_ashrrev_i32_e32 v3, 31, v2
	v_lshl_add_u64 v[2:3], v[2:3], 1, s[0:1]
	global_store_dwordx2 v[2:3], v[6:7], off nt
.Lp4vg_dx:
	s_cmp_lt_i32 s99, 0
	s_cbranch_scc1 .Lp4vg_dy
	s_add_i32 s4, s99, s47
	s_lshr_b32 s0, s4, 31
	s_add_i32 s0, s4, s0
	s_ashr_i32 s101, s0, 1
	s_ashr_i32 s0, s0, 11
	s_and_b32 s1, s101, 0x3ff
	s_ashr_i32 s3, s0, 31
	s_lshl_b32 s0, s0, 10
	v_pk_mul_f32 v[242:243], v[242:243], s[2:3] op_sel_hi:[1,0]
	v_pk_mul_f32 v[244:245], v[244:245], s[2:3] op_sel_hi:[1,0]
	v_pk_mul_f32 v[246:247], v[246:247], s[2:3] op_sel_hi:[1,0]
	v_pk_mul_f32 v[248:249], v[248:249], s[2:3] op_sel_hi:[1,0]
	s_or_b32 s0, s0, s1
	v_cvt_pk_fp8_f32 v242, v242, v246
	s_mul_hi_u32 s1, s0, 0x2100
	s_mulk_i32 s3, 0x2100
	v_cvt_pk_fp8_f32 v242, v243, v247 op_sel:[0,0,1]
	s_add_i32 s1, s1, s3
	s_mulk_i32 s0, 0x2100
	v_cvt_pk_fp8_f32 v243, v244, v248
	v_readlane_b32 s100, v251, 49
	s_add_u32 s0, s100, s0
	v_readlane_b32 s100, v251, 31
	s_addc_u32 s1, s100, s1
	v_cvt_pk_fp8_f32 v243, v245, v249 op_sel:[0,0,1]
	v_lshl_or_b32 v14, s4, 11, v208
	s_lshl_b32 s3, s101, 12
	v_subrev_u32_e32 v2, s3, v14
	v_ashrrev_i32_e32 v3, 31, v2
	v_lshl_add_u64 v[2:3], v[2:3], 1, s[0:1]
	global_store_dwordx2 v[2:3], v[242:243], off nt
.Lp4vg_dy:
.LBB0_554:
	v_readlane_b32 s36, v251, 25
	v_readlane_b32 s39, v251, 28
	v_readlane_b32 s37, v251, 26
	v_readlane_b32 s38, v251, 27
	s_cmp_lt_u32 s39, 6
	s_cbranch_scc1 .LBB0_608
	s_waitcnt vmcnt(0)
	s_barrier
	s_mov_b64 s[0:1], exec
	v_readlane_b32 s2, v251, 23
	v_readlane_b32 s3, v251, 24
	s_and_b64 s[2:3], s[0:1], s[2:3]
	s_mov_b64 exec, s[2:3]
	s_cbranch_execz .LBB0_607
	s_add_u32 s2, s36, 0x4200
	s_addc_u32 s3, s37, 0
	s_add_i32 s4, 0, 0x20160
	v_mov_b32_e32 v1, s4
	s_waitcnt vmcnt(0) expcnt(0) lgkmcnt(0)
	ds_read_b32 v3, v1
	s_add_i32 s4, 0, 0x20164
	v_mov_b32_e32 v1, s4
	ds_read_b32 v1, v1
	s_waitcnt lgkmcnt(1)
	v_cmp_ne_u32_e32 vcc, 0, v3
	s_cbranch_vccnz .LBB0_571
	s_add_u32 s4, s36, 0x4400
	s_addc_u32 s5, s37, 0
	s_add_u32 s6, s36, 0x4500
	s_addc_u32 s7, s37, 0
	s_add_u32 s8, s36, 0x4600
	s_addc_u32 s9, s37, 0
	s_add_u32 s10, s36, 0x4700
	s_addc_u32 s11, s37, 0
	s_add_u32 s12, s36, 0x4800
	s_addc_u32 s13, s37, 0
	s_add_u32 s14, s36, 0x4900
	s_addc_u32 s15, s37, 0
	s_add_u32 s16, s36, 0x4a00
	s_addc_u32 s17, s37, 0
	s_add_u32 s18, s36, 0x4b00
	s_addc_u32 s19, s37, 0
	s_add_u32 s20, s36, 0x4c00
	s_addc_u32 s21, s37, 0
	s_add_u32 s22, s36, 0x4d00
	s_addc_u32 s23, s37, 0
	s_add_u32 s24, s36, 0x4e00
	s_addc_u32 s25, s37, 0
	s_add_u32 s30, s36, 0x4f00
	s_addc_u32 s31, s37, 0
	v_readlane_b32 s26, v251, 0
	s_add_u32 s34, s36, 0x5000
	s_mov_b64 s[42:43], s[38:39]
	v_readlane_b32 s27, v251, 1
	s_addc_u32 s35, s37, 0
	s_mov_b64 s[40:41], s[36:37]
	s_load_dwordx2 s[42:43], s[26:27], 0x4
	s_add_u32 s36, s40, 0x5100
	s_addc_u32 s37, s41, 0
	s_add_u32 s38, s40, 0x5200
	s_addc_u32 s39, s41, 0
	v_readlane_b32 s33, v251, 2
	s_add_u32 s40, s40, 0x5300
	s_waitcnt lgkmcnt(0)
	s_mul_i32 s33, s42, s33
	s_addc_u32 s41, s41, 0
	s_mul_i32 s33, s33, s43
	s_mov_b32 s48, 1
	v_mov_b32_e32 v17, 0
	s_branch .LBB0_559
